# baseline (speedup 1.0000x reference)
.LBB1_39:
	s_or_b64 exec, exec, s[6:7]
	s_movk_i32 s3, 0xbf
	v_cmp_lt_u32_e64 s[6:7], s3, v0
	s_movk_i32 s3, 0xc0
	v_cmp_gt_u32_e32 vcc, s3, v0
	s_and_saveexec_b64 s[8:9], vcc
	s_setprio 3
	s_or_b64 exec, exec, s[8:9]
	v_mul_u32_u24_e32 v126, 0x90, v189
	s_add_i32 s16, 0, 0x24400
	v_lshlrev_b32_e32 v191, 2, v122
	v_lshl_add_u32 v126, v126, 1, 0
	v_lshlrev_b32_e32 v192, 3, v122
	v_lshlrev_b32_e32 v122, 4, v122
	v_lshl_or_b32 v127, v124, 4, v189
	v_lshl_add_u32 v196, v1, 4, s16
	s_movk_i32 s12, 0xff70
	v_lshlrev_b32_e32 v190, 4, v128
	v_add_u32_e32 v193, v126, v122
	v_mul_i32_i24_e32 v127, 0xd0, v127
	v_lshl_add_u32 v197, v124, 10, v196
	v_mad_i32_i24 v124, v189, s12, v126
	v_lshlrev_b32_e32 v126, 6, v128
	v_add3_u32 v194, 0, v127, v122
	v_mul_u32_u24_e32 v127, 0xe0, v189
	s_add_i32 s24, 0, 0x20c00
	v_add3_u32 v198, 0, v126, v122
	v_or_b32_e32 v126, v190, v189
	v_add3_u32 v195, s24, v127, v122
	v_mul_u32_u24_e32 v127, 0x110, v126
	v_add3_u32 v199, 0, v127, v122
	v_lshlrev_b32_e32 v127, 5, v128
	v_add3_u32 v200, v124, v127, v192
	v_lshl_add_u32 v132, v189, 6, v124
	v_add_u32_e32 v202, v124, v122
	v_or_b32_e32 v124, v191, v190
	s_movk_i32 s20, 0x50
	v_lshl_add_u32 v203, v0, 4, s16
	v_cmp_gt_u32_e64 s[16:17], 40, v124
	v_mad_u32_u24 v124, v189, s20, v132
	v_add3_u32 v205, v124, v127, v192
	v_add_u32_e32 v206, v124, v122
	v_and_b32_e32 v124, 0xc0, v0
	s_add_i32 s54, 0, 0x15400
	v_lshl_add_u32 v207, v124, 4, v196
	v_add_u16_e32 v124, -3, v128
	s_movk_i32 s22, 0xab
	v_add3_u32 v204, s54, v127, v192
	v_mul_lo_u16_sdwa v127, v124, s22 dst_sel:DWORD dst_unused:UNUSED_PAD src0_sel:BYTE_0 src1_sel:DWORD
	v_lshrrev_b16_e32 v127, 9, v127
	v_add_u32_e32 v201, v132, v122
	v_mul_lo_u16_e32 v132, 3, v127
	v_sub_u16_e32 v124, v124, v132
	v_and_b32_e32 v124, 0xff, v124
	v_lshl_or_b32 v132, v124, 4, v189
	v_mul_u32_u24_e32 v132, 0xd0, v132
	v_add3_u32 v208, 0, v132, v122
	v_lshl_or_b32 v132, v127, 4, v189
	v_mul_u32_u24_e32 v132, 0xe0, v132
	v_lshlrev_b32_e32 v117, 1, v117
	v_lshlrev_b32_e32 v121, 1, v121
	v_add3_u32 v209, s24, v132, v122
	v_mad_u32_u24 v124, v127, 3, v124
	v_add_u32_e32 v213, s24, v117
	v_add_u32_e32 v214, s24, v121
	s_add_i32 s24, 0, 0x1c400
	v_lshl_add_u32 v210, v124, 10, v196
	v_add_u32_e32 v124, 2, v128
	v_lshl_add_u32 v221, v115, 1, s24
	v_lshl_add_u32 v222, v116, 1, s24
	v_lshl_add_u32 v225, v114, 2, 0
	v_add_u32_e32 v227, s24, v122
	v_add3_u32 v114, v123, v131, v0
	s_mul_i32 s24, s2, 0x6900
	v_mul_u32_u24_e32 v115, 0x690, v130
	v_mul_lo_u16_e32 v127, 0x56, v124
	v_mov_b32_e32 v132, 3
	v_add3_u32 v114, v114, s24, v115
	v_min_u32_e32 v115, 0xc0, v0
	v_mul_lo_u16_sdwa v127, v127, v132 dst_sel:DWORD dst_unused:UNUSED_PAD src0_sel:BYTE_1 src1_sel:DWORD
	v_sub_u32_e32 v114, v114, v115
	v_sub_u16_e32 v127, v124, v127
	v_add_u32_e32 v154, 0x8c, v114
	v_add_u32_e32 v114, v125, v0
	v_mul_u32_u24_e32 v116, 0x690, v129
	v_lshlrev_b16_e32 v127, 4, v127
	s_movk_i32 s25, 0xf0
	v_add3_u32 v114, v114, s24, v116
	v_and_or_b32 v127, v127, s25, v189
	v_add_u32_e32 v224, s54, v121
	v_ashrrev_i32_e32 v121, 31, v120
	v_sub_u32_e32 v114, v114, v115
	s_mul_i32 s25, s2, 0x18000
	v_add_u32_e32 v156, 0x8c, v114
	v_lshl_add_u64 v[158:159], v[120:121], 2, s[40:41]
	v_lshl_add_u64 v[160:161], v[118:119], 2, s[40:41]
	s_movk_i32 s40, 0x1800
	v_mov_b32_e32 v114, s25
	v_mad_u32_u24 v114, v189, s40, v114
	v_or_b32_e32 v229, v114, v190
	v_mul_u32_u24_e32 v114, 0x690, v189
	v_add3_u32 v230, s24, v114, v190
	v_lshl_add_u32 v114, v128, 3, 0
	s_movk_i32 s10, 0x180
	v_cmp_eq_u32_e32 vcc, 2, v128
	v_cmp_gt_u32_e64 s[12:13], 16, v1
	v_lshlrev_b32_e32 v126, 7, v126
	s_movk_i32 s20, 0x300
	s_movk_i32 s22, 0x1c0
	v_mul_u32_u24_e32 v127, 0xd0, v127
	v_add_u32_e32 v231, 0x27400, v114
	v_mov_b32_e32 v114, 0
	s_movk_i32 s3, 0x90
	s_mov_b32 s33, 0
	v_cmp_ne_u32_e64 s[8:9], 3, v128
	v_cmp_gt_u32_e64 s[10:11], s10, v0
	s_movk_i32 s52, 0xd0
	s_movk_i32 s53, 0xe0
	s_and_b64 s[14:15], vcc, s[12:13]
	v_cmp_eq_u32_e64 s[18:19], 0, v1
	v_cmp_gt_u32_e64 s[20:21], s20, v0
	v_cmp_gt_u32_e64 s[22:23], s22, v0
	v_add3_u32 v211, 0, v127, v122
	v_lshl_add_u32 v212, v124, 10, v196
	v_add_u32_e32 v215, 0xe00, v213
	v_add_u32_e32 v216, 0x1c00, v213
	v_add_u32_e32 v217, 0x2a00, v213
	v_add_u32_e32 v218, 0xe00, v214
	v_add_u32_e32 v219, 0x1c00, v214
	v_add_u32_e32 v220, 0x2a00, v214
	v_add_u32_e32 v223, s54, v117
	v_add_u32_e32 v226, s54, v122
	v_sub_u32_e32 v228, v199, v126
	s_mov_b64 s[40:41], 0
	s_mov_b32 s55, 0xf149f2ca
	s_mov_b32 s56, 1.0
	s_movk_i32 s57, 0x46
	s_movk_i32 s58, 0x69
	v_mov_b32_e32 v232, 0x42200000
	s_mov_b32 s59, 0
	v_mov_b32_e32 v162, 0
	v_mov_b32_e32 v163, v114
	v_mov_b32_e32 v164, v114
	v_mov_b32_e32 v165, v114
	v_mov_b32_e32 v168, 0
	v_mov_b32_e32 v169, v114
	v_mov_b32_e32 v170, 0
	v_mov_b32_e32 v171, v114
	s_mov_b32 s75, 0
	s_and_b64 s[72:73], exec, s[6:7]
	s_cbranch_scc1 .Lwf_skip
	ds_read_b128 v[178:181], v228 offset:22272
	ds_read_b128 v[182:185], v228 offset:22336
	s_waitcnt lgkmcnt(0)
.Lwf_skip:
	s_branch .LBB1_43

.LBB1_55:
	s_or_saveexec_b64 s[24:25], s[24:25]
	v_mov_b32_e32 v116, 0
	v_lshlrev_b32_e32 v234, 1, v190
	v_lshlrev_b32_e32 v235, 1, v191
	v_mov_b32_e32 v117, 0
	v_mov_b32_e32 v166, 0
	v_mov_b32_e32 v167, 0
	v_mov_b32_e32 v150, 0
	v_mov_b32_e32 v151, 0
	v_mov_b32_e32 v152, 0
	v_mov_b32_e32 v153, 0
	v_mov_b32_e32 v174, 0
	v_mov_b32_e32 v175, 0
	v_mov_b32_e32 v172, 0
	v_mov_b32_e32 v173, 0
	s_xor_b64 exec, exec, s[24:25]
	s_cbranch_execz .LBB1_57
	s_lshl_b32 s42, s46, 1
	v_add_u32_e32 v115, s42, v199
	v_mad_u32_u24 v176, v233, s3, v227
	v_mov_b32_e32 v115, s54
	v_mad_u32_u24 v162, v233, s53, v115
	v_add3_u32 v115, v162, v234, v235
	ds_read_b64 v[132:133], v115 offset:80
	v_mad_u32_u24 v115, v233, s52, v198
	ds_read_b128 v[150:153], v115 offset:60416
	v_mov_b32_e32 v115, s56
	s_waitcnt lgkmcnt(5)
	v_mfma_f32_16x16x32_bf16 v[240:243], v[86:89], v[146:149], 0
	s_waitcnt lgkmcnt(2)
	v_mfma_f32_16x16x32_bf16 v[124:127], v[124:127], v[138:141], 0
	v_mfma_f32_16x16x32_bf16 v[116:119], v[250:253], v[146:149], v[120:123]
	v_mfma_f32_16x16x32_bf16 v[118:121], v[246:249], v[142:145], v[116:119]
	v_mfma_f32_16x16x32_bf16 v[122:125], v[128:131], v[134:137], v[124:127]
	s_nop 0
	s_waitcnt lgkmcnt(1)
	v_lshlrev_b32_e32 v116, 16, v132
	v_and_b32_e32 v117, 0xffff0000, v132
	v_lshlrev_b32_e32 v166, 16, v133
	v_and_b32_e32 v167, 0xffff0000, v133
	s_nop 2
	v_pk_add_f32 v[172:173], v[120:121], v[124:125]
	v_pk_add_f32 v[174:175], v[118:119], v[122:123]
	v_sub_f32_e32 v119, 1.0, v117
	v_sub_f32_e32 v118, 1.0, v116
	v_sub_f32_e32 v121, 1.0, v167
	v_sub_f32_e32 v120, 1.0, v166
	v_pk_mul_f32 v[120:121], v[172:173], v[120:121]
	v_pk_mul_f32 v[118:119], v[174:175], v[118:119]
	s_waitcnt lgkmcnt(0)
	v_pk_fma_f32 v[122:123], v[152:153], v[166:167], v[120:121]
	v_pk_fma_f32 v[124:125], v[150:151], v[116:117], v[118:119]
	v_mfma_f32_16x16x32_bf16 v[118:121], v[2:5], v[146:149], 0
	v_cndmask_b32_e64 v115, v123, v115, s[14:15]
	v_cndmask_b32_e64 v123, v122, v122, s[14:15]
	v_cndmask_b32_e64 v122, v125, v125, s[14:15]
	v_cndmask_b32_e64 v124, v124, v124, s[14:15]
	v_cvt_pk_bf16_f32 v122, v124, v122
	v_cvt_pk_bf16_f32 v123, v123, v115
	ds_write_b64 v200, v[122:123] offset:58112
	s_and_saveexec_b64 s[72:73], s[18:19]
	v_mov_b32_e32 v115, 0xe380
	ds_add_u32 v115, v115
	s_or_b64 exec, exec, s[72:73]
	v_mfma_f32_16x16x32_bf16 v[118:121], v[6:9], v[142:145], v[118:121]
	v_lshl_add_u32 v115, v192, 1, v162
	ds_read_b128 v[130:133], v115 offset:128
	ds_read_b128 v[236:239], v176 offset:2304
	v_add_u32_e32 v115, s42, v228
	ds_read_b128 v[162:165], v115 offset:39168
	ds_read_b128 v[244:247], v115 offset:39232
	v_mfma_f32_16x16x32_bf16 v[118:121], v[10:13], v[138:141], v[118:121]
	v_mfma_f32_16x16x32_bf16 v[118:121], v[14:17], v[134:137], v[118:121]
	s_waitcnt lgkmcnt(1)
	v_mfma_f32_16x16x32_bf16 v[162:165], v[162:165], v[236:239], 0
	ds_read_b128 v[236:239], v176 offset:2368
	v_mfma_f32_16x16x32_bf16 v[126:129], v[26:29], v[130:133], v[118:121]
	v_mfma_f32_16x16x32_bf16 v[118:121], v[30:33], v[146:149], 0
	v_mfma_f32_16x16x32_bf16 v[122:125], v[58:61], v[146:149], 0
	v_mfma_f32_16x16x32_bf16 v[118:121], v[34:37], v[142:145], v[118:121]
	v_mfma_f32_16x16x32_bf16 v[122:125], v[62:65], v[142:145], v[122:125]
	s_waitcnt lgkmcnt(0)
	v_mfma_f32_16x16x32_bf16 v[162:165], v[244:247], v[236:239], v[162:165]
	v_mov_b32_e32 v246, 0xe380
	ds_read_b32 v246, v246
	ds_read_b128 v[158:161], v202 offset:58112
	ds_read_b128 v[250:253], v202 offset:58176
	ds_read_b128 v[154:157], v203
	v_mfma_f32_16x16x32_bf16 v[236:239], v[90:93], v[142:145], v[240:243]
	v_mfma_f32_16x16x32_bf16 v[118:121], v[38:41], v[138:141], v[118:121]
	s_nop 5
	v_med3_f32 v115, v162, s55, 0
	v_exp_f32_e32 v162, v115
	v_med3_f32 v115, v163, s55, 0
	v_mfma_f32_16x16x32_bf16 v[122:125], v[66:69], v[138:141], v[122:125]
	v_exp_f32_e32 v163, v115
	v_med3_f32 v115, v164, s55, 0
	v_exp_f32_e32 v164, v115
	v_mfma_f32_16x16x32_bf16 v[236:239], v[94:97], v[138:141], v[236:239]
	v_med3_f32 v115, v165, s55, 0
	v_exp_f32_e32 v165, v115
	v_mfma_f32_16x16x32_bf16 v[118:121], v[42:45], v[134:137], v[118:121]
	v_mfma_f32_16x16x32_bf16 v[122:125], v[70:73], v[134:137], v[122:125]
	v_mfma_f32_16x16x32_bf16 v[236:239], v[98:101], v[134:137], v[236:239]
	v_mfma_f32_16x16x32_bf16 v[118:121], v[54:57], v[130:133], v[118:121]
	v_mfma_f32_16x16x32_bf16 v[122:125], v[82:85], v[130:133], v[122:125]
	v_mfma_f32_16x16x32_bf16 v[130:133], v[110:113], v[130:133], v[236:239]

.LBB1_68:
	s_andn2_saveexec_b64 s[24:25], s[24:25]
	s_cbranch_execz .LBB1_80
	s_add_u32 s75, s75, 0x2aa80
	v_readfirstlane_b32 s74, v246
	s_nop 1
	s_cmp_lt_u32 s74, s75
	s_cbranch_scc0 .Lpoll_done_0
.Lpoll_0:
	v_mov_b32_e32 v115, 0xe380
	ds_read_b32 v115, v115
	s_waitcnt lgkmcnt(0)
	v_readfirstlane_b32 s74, v115
	s_nop 1
	s_cmp_lt_u32 s74, s75
	s_cbranch_scc1 .Lpoll_0
	ds_read_b128 v[158:161], v202 offset:58112
	ds_read_b128 v[250:253], v202 offset:58176
	s_waitcnt lgkmcnt(0)
.Lpoll_done_0:
	v_pk_mul_f32 v[176:177], v[166:167], v[152:153]
	v_pk_mul_f32 v[240:241], v[116:117], v[150:151]
	v_mfma_f32_16x16x32_bf16 v[134:137], v[178:181], v[158:161], 0
	v_add_f32_e64 v242, -v116, 1.0
	v_add_f32_e64 v243, -v117, 1.0
	s_waitcnt lgkmcnt(0)
	v_pk_add_f32 v[144:145], v[154:155], 1.0 op_sel_hi:[1,0] neg_lo:[1,0] neg_hi:[1,0]
	v_mfma_f32_16x16x32_bf16 v[140:143], v[182:185], v[250:253], 0
	s_nop 7
	v_pk_add_f32 v[138:139], v[136:137], v[142:143]
	v_pk_add_f32 v[142:143], v[134:135], v[140:141]
	v_pk_mul_f32 v[136:137], v[156:157], v[138:139]
	v_pk_mul_f32 v[134:135], v[154:155], v[142:143]
	v_pk_add_f32 v[140:141], v[156:157], 1.0 op_sel_hi:[1,0] neg_lo:[1,0] neg_hi:[1,0]
	v_pk_fma_f32 v[144:145], v[174:175], v[144:145], v[134:135]
	v_pk_fma_f32 v[140:141], v[172:173], v[140:141], v[136:137]
	v_pk_add_f32 v[136:137], v[166:167], 1.0 op_sel_hi:[1,0] neg_lo:[1,0] neg_hi:[1,0]
	v_pk_fma_f32 v[134:135], v[242:243], v[144:145], v[240:241]
	v_pk_fma_f32 v[136:137], v[136:137], v[140:141], v[176:177]
	s_and_saveexec_b64 s[42:43], s[16:17]
	s_cbranch_execz .LBB1_71
	v_mov_b32_e32 v115, s56
	v_cndmask_b32_e64 v115, v137, v115, s[14:15]
	v_cndmask_b32_e64 v147, v136, v136, s[14:15]
	v_cndmask_b32_e64 v146, v135, v135, s[14:15]
	v_cndmask_b32_e64 v148, v134, v134, s[14:15]
	v_cvt_pk_bf16_f32 v146, v148, v146
	v_cvt_pk_bf16_f32 v147, v147, v115
	v_mad_u32_u24 v115, v233, s53, v204
	ds_write_b64 v115, v[146:147]

.LBB1_91:
	s_or_saveexec_b64 s[24:25], s[24:25]
	v_mov_b32_e32 v116, 0
	v_mov_b32_e32 v117, 0
	v_mov_b32_e32 v172, 0
	v_mov_b32_e32 v173, 0
	v_mov_b32_e32 v150, 0
	v_mov_b32_e32 v151, 0
	v_mov_b32_e32 v152, 0
	v_mov_b32_e32 v153, 0
	v_mov_b32_e32 v176, 0
	v_mov_b32_e32 v177, 0
	v_mov_b32_e32 v174, 0
	v_mov_b32_e32 v175, 0
	s_xor_b64 exec, exec, s[24:25]
	s_cbranch_execz .LBB1_93
	s_lshl_b32 s42, s46, 1
	v_add_u32_e32 v115, s42, v199
	v_mul_u32_u24_e32 v132, 0xe0, v233
	v_add_u32_e32 v115, s54, v132
	v_add_u32_e32 v162, 0xe00, v115
	v_add3_u32 v115, v162, v234, v235
	ds_read_b64 v[132:133], v115 offset:80
	v_mad_u32_u24 v115, v167, s52, v198
	ds_read_b128 v[150:153], v115 offset:60416
	s_waitcnt lgkmcnt(5)
	v_mfma_f32_16x16x32_bf16 v[240:243], v[86:89], v[146:149], 0
	s_waitcnt lgkmcnt(2)
	v_mfma_f32_16x16x32_bf16 v[116:119], v[250:253], v[146:149], v[120:123]
	v_mfma_f32_16x16x32_bf16 v[124:127], v[124:127], v[138:141], 0
	v_mfma_f32_16x16x32_bf16 v[118:121], v[246:249], v[142:145], v[116:119]
	v_mfma_f32_16x16x32_bf16 v[122:125], v[128:131], v[134:137], v[124:127]
	s_nop 0
	s_waitcnt lgkmcnt(1)
	v_lshlrev_b32_e32 v116, 16, v132
	v_and_b32_e32 v117, 0xffff0000, v132
	v_lshlrev_b32_e32 v172, 16, v133
	v_and_b32_e32 v173, 0xffff0000, v133
	v_mov_b32_e32 v115, s56
	s_nop 3
	v_pk_add_f32 v[174:175], v[120:121], v[124:125]
	v_pk_add_f32 v[176:177], v[118:119], v[122:123]
	v_sub_f32_e32 v119, 1.0, v117
	v_sub_f32_e32 v118, 1.0, v116
	v_sub_f32_e32 v121, 1.0, v173
	v_sub_f32_e32 v120, 1.0, v172
	v_pk_mul_f32 v[120:121], v[174:175], v[120:121]
	v_pk_mul_f32 v[118:119], v[176:177], v[118:119]
	s_waitcnt lgkmcnt(0)
	v_pk_fma_f32 v[122:123], v[152:153], v[172:173], v[120:121]
	v_pk_fma_f32 v[124:125], v[150:151], v[116:117], v[118:119]
	v_mfma_f32_16x16x32_bf16 v[118:121], v[2:5], v[146:149], 0
	v_cndmask_b32_e64 v115, v123, v115, s[14:15]
	v_cndmask_b32_e64 v123, v122, v122, s[14:15]
	v_cndmask_b32_e64 v122, v125, v125, s[14:15]
	v_cndmask_b32_e64 v124, v124, v124, s[14:15]
	v_cvt_pk_bf16_f32 v122, v124, v122
	v_cvt_pk_bf16_f32 v123, v123, v115
	ds_write_b64 v200, v[122:123] offset:58112
	s_and_saveexec_b64 s[72:73], s[18:19]
	v_mov_b32_e32 v115, 0xe380
	ds_add_u32 v115, v115
	s_or_b64 exec, exec, s[72:73]
	v_mfma_f32_16x16x32_bf16 v[118:121], v[6:9], v[142:145], v[118:121]
	v_lshl_add_u32 v115, v192, 1, v162
	ds_read_b128 v[130:133], v115 offset:128
	v_add_u32_e32 v115, s42, v228
	ds_read_b128 v[162:165], v115 offset:39168
	ds_read_b128 v[244:247], v115 offset:39232
	s_add_i32 s42, s33, 32
	s_and_b32 s42, s42, 0x60
	v_mfma_f32_16x16x32_bf16 v[118:121], v[10:13], v[138:141], v[118:121]
	v_or_b32_e32 v236, s42, v189
	v_mad_u32_u24 v248, v236, s3, v227
	ds_read_b128 v[236:239], v248
	v_mfma_f32_16x16x32_bf16 v[118:121], v[14:17], v[134:137], v[118:121]
	s_waitcnt lgkmcnt(0)
	v_mfma_f32_16x16x32_bf16 v[162:165], v[162:165], v[236:239], 0
	ds_read_b128 v[236:239], v248 offset:64
	v_mfma_f32_16x16x32_bf16 v[126:129], v[26:29], v[130:133], v[118:121]
	v_mfma_f32_16x16x32_bf16 v[118:121], v[30:33], v[146:149], 0
	v_mfma_f32_16x16x32_bf16 v[122:125], v[58:61], v[146:149], 0
	v_mfma_f32_16x16x32_bf16 v[118:121], v[34:37], v[142:145], v[118:121]
	v_mfma_f32_16x16x32_bf16 v[122:125], v[62:65], v[142:145], v[122:125]
	s_waitcnt lgkmcnt(0)
	v_mfma_f32_16x16x32_bf16 v[162:165], v[244:247], v[236:239], v[162:165]
	v_mov_b32_e32 v246, 0xe380
	ds_read_b32 v246, v246
	ds_read_b128 v[158:161], v202 offset:58112
	ds_read_b128 v[250:253], v202 offset:58176
	ds_read_b128 v[154:157], v207 offset:3072
	v_mfma_f32_16x16x32_bf16 v[236:239], v[90:93], v[142:145], v[240:243]
	v_mfma_f32_16x16x32_bf16 v[118:121], v[38:41], v[138:141], v[118:121]
	s_nop 5
	v_med3_f32 v115, v162, s55, 0
	v_exp_f32_e32 v162, v115
	v_med3_f32 v115, v163, s55, 0
	v_mfma_f32_16x16x32_bf16 v[122:125], v[66:69], v[138:141], v[122:125]
	v_exp_f32_e32 v163, v115
	v_med3_f32 v115, v164, s55, 0
	v_exp_f32_e32 v164, v115
	v_mfma_f32_16x16x32_bf16 v[236:239], v[94:97], v[138:141], v[236:239]
	v_med3_f32 v115, v165, s55, 0
	v_exp_f32_e32 v165, v115
	v_mfma_f32_16x16x32_bf16 v[118:121], v[42:45], v[134:137], v[118:121]
	v_mfma_f32_16x16x32_bf16 v[122:125], v[70:73], v[134:137], v[122:125]
	v_mfma_f32_16x16x32_bf16 v[236:239], v[98:101], v[134:137], v[236:239]
	v_mfma_f32_16x16x32_bf16 v[118:121], v[54:57], v[130:133], v[118:121]
	v_mfma_f32_16x16x32_bf16 v[122:125], v[82:85], v[130:133], v[122:125]
	v_mfma_f32_16x16x32_bf16 v[130:133], v[110:113], v[130:133], v[236:239]

.Lpoll_done_1:
	v_pk_mul_f32 v[240:241], v[172:173], v[152:153]
	v_pk_mul_f32 v[242:243], v[116:117], v[150:151]
	v_mfma_f32_16x16x32_bf16 v[134:137], v[178:181], v[158:161], 0
	v_add_f32_e64 v244, -v116, 1.0
	v_add_f32_e64 v245, -v117, 1.0
	s_waitcnt lgkmcnt(0)
	v_pk_add_f32 v[144:145], v[154:155], 1.0 op_sel_hi:[1,0] neg_lo:[1,0] neg_hi:[1,0]
	v_mfma_f32_16x16x32_bf16 v[140:143], v[182:185], v[250:253], 0
	s_nop 7
	v_pk_add_f32 v[138:139], v[136:137], v[142:143]
	v_pk_add_f32 v[142:143], v[134:135], v[140:141]
	v_pk_mul_f32 v[136:137], v[156:157], v[138:139]
	v_pk_mul_f32 v[134:135], v[154:155], v[142:143]
	v_pk_add_f32 v[140:141], v[156:157], 1.0 op_sel_hi:[1,0] neg_lo:[1,0] neg_hi:[1,0]
	v_pk_fma_f32 v[144:145], v[176:177], v[144:145], v[134:135]
	v_pk_fma_f32 v[140:141], v[174:175], v[140:141], v[136:137]
	v_pk_add_f32 v[136:137], v[172:173], 1.0 op_sel_hi:[1,0] neg_lo:[1,0] neg_hi:[1,0]
	v_pk_fma_f32 v[134:135], v[244:245], v[144:145], v[242:243]
	v_pk_fma_f32 v[136:137], v[136:137], v[140:141], v[240:241]
	s_and_saveexec_b64 s[42:43], s[16:17]
	s_cbranch_execz .LBB1_107
	v_mov_b32_e32 v115, s56
	v_cndmask_b32_e64 v115, v137, v115, s[14:15]
	v_cndmask_b32_e64 v147, v136, v136, s[14:15]
	v_cndmask_b32_e64 v146, v135, v135, s[14:15]
	v_cndmask_b32_e64 v148, v134, v134, s[14:15]
	v_cvt_pk_bf16_f32 v146, v148, v146
	v_cvt_pk_bf16_f32 v147, v147, v115
	v_mad_u32_u24 v115, v167, s53, v204
	ds_write_b64 v115, v[146:147]

.LBB1_127:
	s_or_saveexec_b64 s[24:25], s[24:25]
	v_mov_b32_e32 v116, 0
	v_mov_b32_e32 v117, 0
	v_mov_b32_e32 v172, 0
	v_mov_b32_e32 v173, 0
	v_mov_b32_e32 v150, 0
	v_mov_b32_e32 v151, 0
	v_mov_b32_e32 v152, 0
	v_mov_b32_e32 v153, 0
	v_mov_b32_e32 v176, 0
	v_mov_b32_e32 v177, 0
	v_mov_b32_e32 v174, 0
	v_mov_b32_e32 v175, 0
	s_xor_b64 exec, exec, s[24:25]
	s_cbranch_execz .LBB1_129
	s_lshl_b32 s42, s46, 1
	v_add_u32_e32 v115, s42, v199
	v_mul_u32_u24_e32 v132, 0xe0, v167
	v_add_u32_e32 v115, s54, v132
	v_add_u32_e32 v162, 0xe00, v115
	v_add3_u32 v115, v162, v234, v235
	ds_read_b64 v[132:133], v115 offset:80
	v_mad_u32_u24 v115, v236, s52, v198
	ds_read_b128 v[150:153], v115 offset:60416
	s_waitcnt lgkmcnt(5)
	v_mfma_f32_16x16x32_bf16 v[242:245], v[86:89], v[146:149], 0
	s_waitcnt lgkmcnt(2)
	v_mfma_f32_16x16x32_bf16 v[116:119], v[250:253], v[146:149], v[120:123]
	v_mfma_f32_16x16x32_bf16 v[124:127], v[124:127], v[138:141], 0
	v_mfma_f32_16x16x32_bf16 v[118:121], v[246:249], v[142:145], v[116:119]
	v_mfma_f32_16x16x32_bf16 v[122:125], v[128:131], v[134:137], v[124:127]
	s_nop 0
	s_waitcnt lgkmcnt(1)
	v_lshlrev_b32_e32 v116, 16, v132
	v_and_b32_e32 v117, 0xffff0000, v132
	v_lshlrev_b32_e32 v172, 16, v133
	v_and_b32_e32 v173, 0xffff0000, v133
	v_mov_b32_e32 v115, s56
	s_nop 3
	v_pk_add_f32 v[174:175], v[120:121], v[124:125]
	v_pk_add_f32 v[176:177], v[118:119], v[122:123]
	v_sub_f32_e32 v119, 1.0, v117
	v_sub_f32_e32 v118, 1.0, v116
	v_sub_f32_e32 v121, 1.0, v173
	v_sub_f32_e32 v120, 1.0, v172
	v_pk_mul_f32 v[120:121], v[174:175], v[120:121]
	v_pk_mul_f32 v[118:119], v[176:177], v[118:119]
	s_waitcnt lgkmcnt(0)
	v_pk_fma_f32 v[122:123], v[152:153], v[172:173], v[120:121]
	v_pk_fma_f32 v[124:125], v[150:151], v[116:117], v[118:119]
	v_mfma_f32_16x16x32_bf16 v[118:121], v[2:5], v[146:149], 0
	v_cndmask_b32_e64 v115, v123, v115, s[14:15]
	v_cndmask_b32_e64 v123, v122, v122, s[14:15]
	v_cndmask_b32_e64 v122, v125, v125, s[14:15]
	v_cndmask_b32_e64 v124, v124, v124, s[14:15]
	v_cvt_pk_bf16_f32 v122, v124, v122
	v_cvt_pk_bf16_f32 v123, v123, v115
	ds_write_b64 v200, v[122:123] offset:58112
	s_and_saveexec_b64 s[72:73], s[18:19]
	v_mov_b32_e32 v115, 0xe380
	ds_add_u32 v115, v115
	s_or_b64 exec, exec, s[72:73]
	v_mfma_f32_16x16x32_bf16 v[118:121], v[6:9], v[142:145], v[118:121]
	v_lshl_add_u32 v115, v192, 1, v162
	ds_read_b128 v[130:133], v115 offset:128
	v_add_u32_e32 v115, s42, v228
	ds_read_b128 v[162:165], v115 offset:39168
	ds_read_b128 v[246:249], v115 offset:39232
	s_add_i32 s42, s33, 32
	s_and_b32 s42, s42, 0x60
	v_mfma_f32_16x16x32_bf16 v[118:121], v[10:13], v[138:141], v[118:121]
	v_or_b32_e32 v167, s42, v189
	v_mad_u32_u24 v167, v167, s3, v227
	ds_read_b128 v[238:241], v167 offset:2304
	v_mfma_f32_16x16x32_bf16 v[118:121], v[14:17], v[134:137], v[118:121]
	s_waitcnt lgkmcnt(0)
	v_mfma_f32_16x16x32_bf16 v[162:165], v[162:165], v[238:241], 0
	ds_read_b128 v[238:241], v167 offset:2368
	v_mfma_f32_16x16x32_bf16 v[126:129], v[26:29], v[130:133], v[118:121]
	v_mfma_f32_16x16x32_bf16 v[118:121], v[30:33], v[146:149], 0
	v_mfma_f32_16x16x32_bf16 v[122:125], v[58:61], v[146:149], 0
	v_mfma_f32_16x16x32_bf16 v[118:121], v[34:37], v[142:145], v[118:121]
	v_mfma_f32_16x16x32_bf16 v[122:125], v[62:65], v[142:145], v[122:125]
	s_waitcnt lgkmcnt(0)
	v_mfma_f32_16x16x32_bf16 v[162:165], v[246:249], v[238:241], v[162:165]
	v_mov_b32_e32 v246, 0xe380
	ds_read_b32 v246, v246
	ds_read_b128 v[158:161], v202 offset:58112
	ds_read_b128 v[250:253], v202 offset:58176
	ds_read_b128 v[154:157], v207 offset:6144
	v_mfma_f32_16x16x32_bf16 v[238:241], v[90:93], v[142:145], v[242:245]
	v_mfma_f32_16x16x32_bf16 v[118:121], v[38:41], v[138:141], v[118:121]
	s_nop 5
	v_med3_f32 v115, v162, s55, 0
	v_exp_f32_e32 v162, v115
	v_med3_f32 v115, v163, s55, 0
	v_mfma_f32_16x16x32_bf16 v[122:125], v[66:69], v[138:141], v[122:125]
	v_exp_f32_e32 v163, v115
	v_med3_f32 v115, v164, s55, 0
	v_exp_f32_e32 v164, v115
	v_mfma_f32_16x16x32_bf16 v[238:241], v[94:97], v[138:141], v[238:241]
	v_med3_f32 v115, v165, s55, 0
	v_exp_f32_e32 v165, v115
	v_mfma_f32_16x16x32_bf16 v[118:121], v[42:45], v[134:137], v[118:121]
	v_mfma_f32_16x16x32_bf16 v[122:125], v[70:73], v[134:137], v[122:125]
	v_mfma_f32_16x16x32_bf16 v[238:241], v[98:101], v[134:137], v[238:241]
	v_mfma_f32_16x16x32_bf16 v[118:121], v[54:57], v[130:133], v[118:121]
	v_mfma_f32_16x16x32_bf16 v[122:125], v[82:85], v[130:133], v[122:125]
	v_mfma_f32_16x16x32_bf16 v[130:133], v[110:113], v[130:133], v[238:241]

.Lpoll_done_2:
	v_pk_mul_f32 v[242:243], v[172:173], v[152:153]
	v_pk_mul_f32 v[244:245], v[116:117], v[150:151]
	v_mfma_f32_16x16x32_bf16 v[134:137], v[178:181], v[158:161], 0
	v_add_f32_e64 v246, -v116, 1.0
	v_add_f32_e64 v247, -v117, 1.0
	s_waitcnt lgkmcnt(0)
	v_pk_add_f32 v[144:145], v[154:155], 1.0 op_sel_hi:[1,0] neg_lo:[1,0] neg_hi:[1,0]
	v_mfma_f32_16x16x32_bf16 v[140:143], v[182:185], v[250:253], 0
	s_nop 7
	v_pk_add_f32 v[138:139], v[136:137], v[142:143]
	v_pk_add_f32 v[142:143], v[134:135], v[140:141]
	v_pk_mul_f32 v[136:137], v[156:157], v[138:139]
	v_pk_mul_f32 v[134:135], v[154:155], v[142:143]
	v_pk_add_f32 v[140:141], v[156:157], 1.0 op_sel_hi:[1,0] neg_lo:[1,0] neg_hi:[1,0]
	v_pk_fma_f32 v[144:145], v[176:177], v[144:145], v[134:135]
	v_pk_fma_f32 v[140:141], v[174:175], v[140:141], v[136:137]
	v_pk_add_f32 v[136:137], v[172:173], 1.0 op_sel_hi:[1,0] neg_lo:[1,0] neg_hi:[1,0]
	v_pk_fma_f32 v[134:135], v[246:247], v[144:145], v[244:245]
	v_pk_fma_f32 v[136:137], v[136:137], v[140:141], v[242:243]
	s_and_saveexec_b64 s[42:43], s[16:17]
	s_cbranch_execz .LBB1_143
	v_mov_b32_e32 v115, s56
	v_cndmask_b32_e64 v115, v137, v115, s[14:15]
	v_cndmask_b32_e64 v147, v136, v136, s[14:15]
	v_cndmask_b32_e64 v146, v135, v135, s[14:15]
	v_cndmask_b32_e64 v148, v134, v134, s[14:15]
	v_cvt_pk_bf16_f32 v146, v148, v146
	v_cvt_pk_bf16_f32 v147, v147, v115
	v_mad_u32_u24 v115, v236, s53, v204
	ds_write_b64 v115, v[146:147]

.LBB1_165:
	s_or_saveexec_b64 s[42:43], s[42:43]
	v_cndmask_b32_e64 v115, 0, 1, s[24:25]
	v_mov_b32_e32 v117, 0
	v_cmp_ne_u32_e64 s[24:25], 1, v115
	v_mov_b32_e32 v116, 0
	v_mov_b32_e32 v177, 0
	v_mov_b32_e32 v176, 0
	v_mov_b32_e32 v153, 0
	v_mov_b32_e32 v152, 0
	v_mov_b32_e32 v151, 0
	v_mov_b32_e32 v150, 0
	v_mov_b32_e32 v173, 0
	v_mov_b32_e32 v172, 0
	v_mov_b32_e32 v175, 0
	v_mov_b32_e32 v174, 0
	s_xor_b64 exec, exec, s[42:43]
	s_cbranch_execz .LBB1_169
	v_lshl_add_u32 v115, s48, 1, v199
	v_mul_u32_u24_e32 v132, 0xe0, v236
	s_and_b64 vcc, exec, s[24:25]
	v_add_u32_e32 v115, s54, v132
	v_add_u32_e32 v132, 0xe00, v115
	v_add3_u32 v115, v132, v234, v235
	s_waitcnt lgkmcnt(0)
	v_mfma_f32_16x16x32_bf16 v[124:127], v[124:127], v[142:145], 0
	v_mfma_f32_16x16x32_bf16 v[116:119], v[250:253], v[134:137], v[120:123]
	v_mfma_f32_16x16x32_bf16 v[118:121], v[246:249], v[138:141], v[116:119]
	s_nop 2
	ds_read_b64 v[116:117], v115 offset:80
	v_mad_u32_u24 v115, v167, s52, v198
	ds_read_b128 v[150:153], v115 offset:60416
	v_mfma_f32_16x16x32_bf16 v[122:125], v[128:131], v[146:149], v[124:127]
	v_mov_b32_e32 v115, s56
	s_waitcnt lgkmcnt(1)
	v_lshlrev_b32_e32 v174, 16, v116
	v_and_b32_e32 v175, 0xffff0000, v116
	v_lshlrev_b32_e32 v172, 16, v117
	v_and_b32_e32 v173, 0xffff0000, v117
	s_nop 1
	v_pk_add_f32 v[116:117], v[120:121], v[124:125]
	v_pk_add_f32 v[176:177], v[118:119], v[122:123]
	v_sub_f32_e32 v119, 1.0, v173
	v_sub_f32_e32 v118, 1.0, v172
	v_sub_f32_e32 v121, 1.0, v175
	v_sub_f32_e32 v120, 1.0, v174
	v_pk_mul_f32 v[120:121], v[176:177], v[120:121]
	v_pk_mul_f32 v[118:119], v[116:117], v[118:119]
	s_waitcnt lgkmcnt(0)
	v_pk_fma_f32 v[124:125], v[150:151], v[174:175], v[120:121]
	v_pk_fma_f32 v[122:123], v[152:153], v[172:173], v[118:119]
	v_cndmask_b32_e64 v124, v124, v124, s[14:15]
	v_cndmask_b32_e64 v115, v123, v115, s[14:15]
	v_cndmask_b32_e64 v123, v122, v122, s[14:15]
	v_cndmask_b32_e64 v122, v125, v125, s[14:15]
	v_cvt_pk_bf16_f32 v122, v124, v122
	v_cvt_pk_bf16_f32 v123, v123, v115
	v_mfma_f32_16x16x32_bf16 v[118:121], v[2:5], v[134:137], 0
	ds_write_b64 v200, v[122:123] offset:58112
	s_and_saveexec_b64 s[72:73], s[18:19]
	v_mov_b32_e32 v115, 0xe380
	ds_add_u32 v115, v115
	s_or_b64 exec, exec, s[72:73]
	v_lshl_add_u32 v115, v192, 1, v132
	v_mfma_f32_16x16x32_bf16 v[122:125], v[30:33], v[134:137], 0
	ds_read_b128 v[130:133], v115 offset:128
	v_mfma_f32_16x16x32_bf16 v[126:129], v[58:61], v[134:137], 0
	v_mfma_f32_16x16x32_bf16 v[234:237], v[86:89], v[134:137], 0
	v_mfma_f32_16x16x32_bf16 v[118:121], v[6:9], v[138:141], v[118:121]
	v_mfma_f32_16x16x32_bf16 v[122:125], v[34:37], v[138:141], v[122:125]
	v_mfma_f32_16x16x32_bf16 v[126:129], v[62:65], v[138:141], v[126:129]
	v_mfma_f32_16x16x32_bf16 v[234:237], v[90:93], v[138:141], v[234:237]
	v_mfma_f32_16x16x32_bf16 v[118:121], v[10:13], v[142:145], v[118:121]
	v_mfma_f32_16x16x32_bf16 v[122:125], v[38:41], v[142:145], v[122:125]
	v_mfma_f32_16x16x32_bf16 v[126:129], v[66:69], v[142:145], v[126:129]
	v_mfma_f32_16x16x32_bf16 v[234:237], v[94:97], v[142:145], v[234:237]
	v_mfma_f32_16x16x32_bf16 v[118:121], v[14:17], v[146:149], v[118:121]
	v_mfma_f32_16x16x32_bf16 v[122:125], v[42:45], v[146:149], v[122:125]
	v_mfma_f32_16x16x32_bf16 v[126:129], v[70:73], v[146:149], v[126:129]
	v_mfma_f32_16x16x32_bf16 v[234:237], v[98:101], v[146:149], v[234:237]
	s_waitcnt lgkmcnt(0)
	v_mfma_f32_16x16x32_bf16 v[118:121], v[26:29], v[130:133], v[118:121]
	v_mov_b32_e32 v246, 0xe380
	ds_read_b32 v246, v246
	ds_read_b128 v[158:161], v202 offset:58112
	ds_read_b128 v[250:253], v202 offset:58176
	ds_read_b128 v[154:157], v207 offset:9216
	v_mfma_f32_16x16x32_bf16 v[122:125], v[54:57], v[130:133], v[122:125]
	v_mfma_f32_16x16x32_bf16 v[126:129], v[82:85], v[130:133], v[126:129]
	v_mfma_f32_16x16x32_bf16 v[130:133], v[110:113], v[130:133], v[234:237]
	s_cbranch_vccnz .LBB1_168
	v_lshl_add_u32 v115, s48, 1, v228
	ds_read_b128 v[162:165], v115 offset:39168
	s_add_i32 s44, s33, 64
	v_and_or_b32 v233, s44, 64, v189
	v_mad_u32_u24 v233, v233, s3, v227
	ds_read_b128 v[234:237], v115 offset:39232
	ds_read_b128 v[238:241], v233
	ds_read_b128 v[242:245], v233 offset:64
	s_waitcnt lgkmcnt(1)
	v_mfma_f32_16x16x32_bf16 v[162:165], v[162:165], v[238:241], 0
	s_waitcnt lgkmcnt(0)
	v_mfma_f32_16x16x32_bf16 v[162:165], v[234:237], v[242:245], v[162:165]
	s_nop 7
	v_med3_f32 v115, v162, s55, 0
	v_med3_f32 v163, v163, s55, 0
	v_med3_f32 v164, v164, s55, 0
	v_med3_f32 v165, v165, s55, 0
	v_exp_f32_e32 v162, v115
	v_exp_f32_e32 v163, v163
	v_exp_f32_e32 v164, v164
	v_exp_f32_e32 v165, v165

.LBB1_180:
	s_andn2_saveexec_b64 s[42:43], s[42:43]
	s_cbranch_execz .LBB1_192
	s_add_u32 s75, s75, 0x2aa80
	v_readfirstlane_b32 s74, v246
	s_nop 1
	s_cmp_lt_u32 s74, s75
	s_cbranch_scc0 .Lpoll_done_3

.Lpoll_done_3:
	v_pk_mul_f32 v[238:239], v[172:173], v[152:153]
	v_pk_mul_f32 v[240:241], v[174:175], v[150:151]
	v_mfma_f32_16x16x32_bf16 v[134:137], v[178:181], v[158:161], 0
	v_add_f32_e64 v242, -v174, 1.0
	v_add_f32_e64 v243, -v175, 1.0
	s_waitcnt lgkmcnt(0)
	v_pk_add_f32 v[144:145], v[154:155], 1.0 op_sel_hi:[1,0] neg_lo:[1,0] neg_hi:[1,0]
	v_mfma_f32_16x16x32_bf16 v[140:143], v[182:185], v[250:253], 0
	s_nop 7
	v_pk_add_f32 v[138:139], v[136:137], v[142:143]
	v_pk_add_f32 v[142:143], v[134:135], v[140:141]
	v_pk_mul_f32 v[136:137], v[156:157], v[138:139]
	v_pk_mul_f32 v[134:135], v[154:155], v[142:143]
	v_pk_add_f32 v[140:141], v[156:157], 1.0 op_sel_hi:[1,0] neg_lo:[1,0] neg_hi:[1,0]
	v_pk_fma_f32 v[144:145], v[176:177], v[144:145], v[134:135]
	v_pk_fma_f32 v[140:141], v[116:117], v[140:141], v[136:137]
	v_pk_add_f32 v[136:137], v[172:173], 1.0 op_sel_hi:[1,0] neg_lo:[1,0] neg_hi:[1,0]
	v_pk_fma_f32 v[134:135], v[242:243], v[144:145], v[240:241]
	v_pk_fma_f32 v[136:137], v[136:137], v[140:141], v[238:239]
	s_and_saveexec_b64 s[44:45], s[16:17]
	s_cbranch_execz .LBB1_183
	v_mov_b32_e32 v115, s56
	v_cndmask_b32_e64 v115, v137, v115, s[14:15]
	v_cndmask_b32_e64 v147, v136, v136, s[14:15]
	v_cndmask_b32_e64 v146, v135, v135, s[14:15]
	v_cndmask_b32_e64 v148, v134, v134, s[14:15]
	v_cvt_pk_bf16_f32 v146, v148, v146
	v_cvt_pk_bf16_f32 v147, v147, v115
	v_mad_u32_u24 v115, v167, s53, v204
	ds_write_b64 v115, v[146:147]
